# GEMM K-loops: 32 LDS-DMA stage issues use the SADDR form (SGPR base + 32-bit lane offset) instead of a VALU 64-bit add into a temp pair
# baseline (speedup 1.0000x reference)
.Lp1vg_mmafter_b:
	s_barrier
	s_mov_b32 m0, s69
	v_lshl_add_u64 v[4:5], v[4:5], 0, s[24:25]
	s_add_u32 s4, s56, 0x80080
	ds_read_b128 v[174:177], v234 offset:49152
	ds_read_b128 v[178:181], v234 offset:50176
	ds_read_b128 v[182:185], v234 offset:51200
	ds_read_b128 v[186:189], v234 offset:52224
	ds_read_b128 v[190:193], v234 offset:53248
	ds_read_b128 v[194:197], v234 offset:54272
	ds_read_b128 v[198:201], v234 offset:55296
	ds_read_b128 v[202:205], v234 offset:56320
	global_load_lds_dwordx4 v[4:5], off
	v_lshl_add_u64 v[4:5], v[226:227], 0, s[24:25]
	s_mov_b32 m0, s70
	s_addc_u32 s5, s57, 0
	global_load_lds_dwordx4 v[4:5], off
	s_mov_b32 m0, s73
	s_nop 0
	global_load_lds_dwordx4 v212, s[4:5]
	s_mov_b32 m0, s75
	s_nop 0
	global_load_lds_dwordx4 v216, s[4:5]
	v_lshl_add_u64 v[4:5], v[228:229], 0, s[24:25]
	s_mov_b32 m0, s71
	s_nop 0
	global_load_lds_dwordx4 v[4:5], off
	v_lshl_add_u64 v[4:5], v[230:231], 0, s[24:25]
	s_mov_b32 m0, s72
	s_nop 0
	global_load_lds_dwordx4 v[4:5], off
	s_cmp_eq_u32 s100, 3
	s_cbranch_scc1 .Lp1vg_w11_b2
	s_cmp_eq_u32 s100, 2
	s_cbranch_scc1 .Lp1vg_wk2_b2
	s_waitcnt vmcnt(8)
	s_branch .Lp1vg_wd_b2

.LBB0_168:
	ds_read_b128 v[158:161], v232
	ds_read_b128 v[162:165], v232 offset:1024
	ds_read_b128 v[166:169], v232 offset:2048
	ds_read_b128 v[170:173], v232 offset:3072
	ds_read_b128 v[142:145], v233
	ds_read_b128 v[146:149], v233 offset:1024
	ds_read_b128 v[150:153], v233 offset:2048
	ds_read_b128 v[154:157], v233 offset:3072
	s_add_i32 m0, s41, 0xc000
	ds_read_b128 v[198:201], v234
	ds_read_b128 v[202:205], v234 offset:1024
	ds_read_b128 v[190:193], v234 offset:2048
	ds_read_b128 v[194:197], v234 offset:3072
	ds_read_b128 v[182:185], v234 offset:4096
	ds_read_b128 v[186:189], v234 offset:5120
	ds_read_b128 v[174:177], v234 offset:6144
	ds_read_b128 v[178:181], v234 offset:7168
	global_load_lds_dwordx4 v218, s[54:55]
	v_lshl_add_u64 v[4:5], s[54:55], 0, v[220:221]
	s_add_i32 m0, s41, 0xe000
	s_nop 0
	global_load_lds_dwordx4 v[4:5], off
	s_cmp_eq_u32 s100, 3
	s_cbranch_scc1 .Lp1vg_w11_a1
	s_cmp_eq_u32 s100, 2
	s_cbranch_scc1 .Lp1vg_wk2_a1
	s_waitcnt vmcnt(8)
	s_branch .Lp1vg_wd_a1

.Lp1vg_mmjoin_a:
	s_barrier
	s_mov_b32 m0, s53
	v_lshl_add_u64 v[4:5], s[56:57], 0, v[212:213]
	s_add_u32 s82, s56, 0x80000
	ds_read_b128 v[174:177], v234 offset:16384
	ds_read_b128 v[178:181], v234 offset:17408
	ds_read_b128 v[182:185], v234 offset:18432
	ds_read_b128 v[186:189], v234 offset:19456
	ds_read_b128 v[190:193], v234 offset:20480
	ds_read_b128 v[194:197], v234 offset:21504
	ds_read_b128 v[198:201], v234 offset:22528
	ds_read_b128 v[202:205], v234 offset:23552
	global_load_lds_dwordx4 v[4:5], off
	v_lshl_add_u64 v[226:227], s[56:57], 0, v[216:217]
	s_mov_b32 m0, s60
	s_addc_u32 s83, s57, 0
	global_load_lds_dwordx4 v[226:227], off
	s_mov_b32 m0, s61
	v_lshl_add_u64 v[230:231], s[4:5], 0, v[214:215]
	global_load_lds_dwordx4 v212, s[82:83]
	s_mov_b32 m0, s64
	s_nop 0
	global_load_lds_dwordx4 v216, s[82:83]
	v_lshl_add_u64 v[228:229], s[4:5], 0, v[210:211]
	s_mov_b32 m0, s41
	s_nop 0
	global_load_lds_dwordx4 v[228:229], off
	s_mov_b32 m0, s65
	s_nop 0
	global_load_lds_dwordx4 v[230:231], off
	s_cmp_eq_u32 s100, 3
	s_cbranch_scc1 .Lp1vg_w11_a2
	s_cmp_eq_u32 s100, 2
	s_cbranch_scc1 .Lp1vg_wk2_a2
	s_waitcnt vmcnt(8)
	s_branch .Lp1vg_wd_a2

.Lp1vg_wd_a2:
	s_waitcnt lgkmcnt(0)
	s_barrier
	s_setprio 1
	s_waitcnt lgkmcnt(0)
	v_mfma_f32_16x16x32_bf16 v[74:77], v[158:161], v[174:177], v[74:77]
	v_mfma_f32_16x16x32_bf16 v[70:73], v[166:169], v[174:177], v[70:73]
	v_mfma_f32_16x16x32_bf16 v[58:61], v[158:161], v[182:185], v[58:61]
	v_mfma_f32_16x16x32_bf16 v[54:57], v[166:169], v[182:185], v[54:57]
	v_mfma_f32_16x16x32_bf16 v[42:45], v[158:161], v[190:193], v[42:45]
	v_mfma_f32_16x16x32_bf16 v[38:41], v[166:169], v[190:193], v[38:41]
	v_mfma_f32_16x16x32_bf16 v[26:29], v[158:161], v[198:201], v[26:29]
	v_mfma_f32_16x16x32_bf16 v[22:25], v[166:169], v[198:201], v[22:25]
	v_mfma_f32_16x16x32_bf16 v[74:77], v[162:165], v[178:181], v[74:77]
	v_mfma_f32_16x16x32_bf16 v[70:73], v[170:173], v[178:181], v[70:73]
	v_mfma_f32_16x16x32_bf16 v[58:61], v[162:165], v[186:189], v[58:61]
	v_mfma_f32_16x16x32_bf16 v[54:57], v[170:173], v[186:189], v[54:57]
	v_mfma_f32_16x16x32_bf16 v[42:45], v[162:165], v[194:197], v[42:45]
	v_mfma_f32_16x16x32_bf16 v[38:41], v[170:173], v[194:197], v[38:41]
	v_mfma_f32_16x16x32_bf16 v[26:29], v[162:165], v[202:205], v[26:29]
	v_mfma_f32_16x16x32_bf16 v[22:25], v[170:173], v[202:205], v[22:25]
	s_setprio 0
	s_setprio 1
	v_mfma_f32_16x16x32_bf16 v[66:69], v[142:145], v[174:177], v[66:69]
	v_mfma_f32_16x16x32_bf16 v[62:65], v[150:153], v[174:177], v[62:65]
	v_mfma_f32_16x16x32_bf16 v[50:53], v[142:145], v[182:185], v[50:53]
	v_mfma_f32_16x16x32_bf16 v[46:49], v[150:153], v[182:185], v[46:49]
	v_mfma_f32_16x16x32_bf16 v[34:37], v[142:145], v[190:193], v[34:37]
	v_mfma_f32_16x16x32_bf16 v[30:33], v[150:153], v[190:193], v[30:33]
	v_mfma_f32_16x16x32_bf16 v[18:21], v[142:145], v[198:201], v[18:21]
	v_mfma_f32_16x16x32_bf16 v[14:17], v[150:153], v[198:201], v[14:17]
	v_mfma_f32_16x16x32_bf16 v[66:69], v[146:149], v[178:181], v[66:69]
	v_mfma_f32_16x16x32_bf16 v[62:65], v[154:157], v[178:181], v[62:65]
	v_mfma_f32_16x16x32_bf16 v[50:53], v[146:149], v[186:189], v[50:53]
	v_mfma_f32_16x16x32_bf16 v[46:49], v[154:157], v[186:189], v[46:49]
	v_mfma_f32_16x16x32_bf16 v[34:37], v[146:149], v[194:197], v[34:37]
	v_mfma_f32_16x16x32_bf16 v[30:33], v[154:157], v[194:197], v[30:33]
	v_mfma_f32_16x16x32_bf16 v[18:21], v[146:149], v[202:205], v[18:21]
	v_mfma_f32_16x16x32_bf16 v[14:17], v[154:157], v[202:205], v[14:17]
	s_setprio 0
	s_barrier
	v_add_u32_e32 v2, 0x18000, v209
	ds_read_b128 v[158:161], v2
	ds_read_b128 v[162:165], v2 offset:1024
	ds_read_b128 v[166:169], v2 offset:2048
	ds_read_b128 v[170:173], v2 offset:3072
	v_add_u32_e32 v2, 0x1c000, v209
	ds_read_b128 v[142:145], v2
	ds_read_b128 v[146:149], v2 offset:1024
	ds_read_b128 v[150:153], v2 offset:2048
	ds_read_b128 v[154:157], v2 offset:3072
	s_add_u32 s4, s4, 0x80000
	s_addc_u32 s5, s5, 0
	s_mov_b32 m0, s66
	ds_read_b128 v[198:201], v234 offset:32768
	ds_read_b128 v[202:205], v234 offset:33792
	ds_read_b128 v[190:193], v234 offset:34816
	ds_read_b128 v[194:197], v234 offset:35840
	ds_read_b128 v[182:185], v234 offset:36864
	ds_read_b128 v[186:189], v234 offset:37888
	ds_read_b128 v[174:177], v234 offset:38912
	ds_read_b128 v[178:181], v234 offset:39936
	global_load_lds_dwordx4 v210, s[4:5]
	v_lshl_add_u64 v[238:239], s[4:5], 0, v[214:215]
	s_mov_b32 m0, s67
	s_nop 0
	global_load_lds_dwordx4 v[238:239], off
	s_cmp_eq_u32 s100, 3
	s_cbranch_scc1 .Lp1vg_w11_b1
	s_cmp_eq_u32 s100, 2
	s_cbranch_scc1 .Lp1vg_wk2_b1
	s_waitcnt vmcnt(8)
	s_branch .Lp1vg_wd_b1

.Lp4vg_mmafter_b:
	s_barrier
	s_mov_b32 m0, s48
	v_lshl_add_u64 v[4:5], v[4:5], 0, s[0:1]
	s_add_u32 s4, s34, 0x80080
	ds_read_b128 v[174:177], v230 offset:49152
	ds_read_b128 v[178:181], v230 offset:50176
	ds_read_b128 v[182:185], v230 offset:51200
	ds_read_b128 v[186:189], v230 offset:52224
	ds_read_b128 v[190:193], v230 offset:53248
	ds_read_b128 v[194:197], v230 offset:54272
	ds_read_b128 v[198:201], v230 offset:55296
	ds_read_b128 v[202:205], v230 offset:56320
	global_load_lds_dwordx4 v[4:5], off
	v_lshl_add_u64 v[4:5], v[222:223], 0, s[0:1]
	s_mov_b32 m0, s49
	s_addc_u32 s5, s35, 0
	global_load_lds_dwordx4 v[4:5], off
	s_mov_b32 m0, s52
	s_nop 0
	global_load_lds_dwordx4 v210, s[4:5]
	s_mov_b32 m0, s53
	s_nop 0
	global_load_lds_dwordx4 v212, s[4:5]
	v_lshl_add_u64 v[4:5], v[224:225], 0, s[0:1]
	s_mov_b32 m0, s50
	s_nop 0
	global_load_lds_dwordx4 v[4:5], off
	v_lshl_add_u64 v[4:5], v[226:227], 0, s[0:1]
	s_mov_b32 m0, s51
	s_nop 0
	global_load_lds_dwordx4 v[4:5], off
	s_cmp_eq_u32 s100, 3
	s_cbranch_scc1 .Lp4vg_w11_b2
	s_cmp_eq_u32 s100, 2
	s_cbranch_scc1 .Lp4vg_wk2_b2
	s_waitcnt vmcnt(8)
	s_branch .Lp4vg_wd_b2

.LBB0_536:
	ds_read_b128 v[158:161], v228
	ds_read_b128 v[162:165], v228 offset:1024
	ds_read_b128 v[166:169], v228 offset:2048
	ds_read_b128 v[170:173], v228 offset:3072
	ds_read_b128 v[142:145], v229
	ds_read_b128 v[146:149], v229 offset:1024
	ds_read_b128 v[150:153], v229 offset:2048
	ds_read_b128 v[154:157], v229 offset:3072
	s_add_i32 m0, s21, 0xc000
	ds_read_b128 v[198:201], v230
	ds_read_b128 v[202:205], v230 offset:1024
	ds_read_b128 v[190:193], v230 offset:2048
	ds_read_b128 v[194:197], v230 offset:3072
	ds_read_b128 v[182:185], v230 offset:4096
	ds_read_b128 v[186:189], v230 offset:5120
	ds_read_b128 v[174:177], v230 offset:6144
	ds_read_b128 v[178:181], v230 offset:7168
	global_load_lds_dwordx4 v214, s[24:25]
	v_lshl_add_u64 v[4:5], s[24:25], 0, v[216:217]
	s_add_i32 m0, s21, 0xe000
	s_nop 0
	global_load_lds_dwordx4 v[4:5], off
	s_cmp_eq_u32 s100, 3
	s_cbranch_scc1 .Lp4vg_w11_a1
	s_cmp_eq_u32 s100, 2
	s_cbranch_scc1 .Lp4vg_wk2_a1
	s_waitcnt vmcnt(8)
	s_branch .Lp4vg_wd_a1

.Lp4vg_mmjoin_a:
	s_barrier
	s_mov_b32 m0, s33
	v_lshl_add_u64 v[4:5], s[34:35], 0, v[210:211]
	s_add_u32 s64, s34, 0x80000
	ds_read_b128 v[174:177], v230 offset:16384
	ds_read_b128 v[178:181], v230 offset:17408
	ds_read_b128 v[182:185], v230 offset:18432
	ds_read_b128 v[186:189], v230 offset:19456
	ds_read_b128 v[190:193], v230 offset:20480
	ds_read_b128 v[194:197], v230 offset:21504
	ds_read_b128 v[198:201], v230 offset:22528
	ds_read_b128 v[202:205], v230 offset:23552
	global_load_lds_dwordx4 v[4:5], off
	v_lshl_add_u64 v[222:223], s[34:35], 0, v[212:213]
	s_mov_b32 m0, s36
	s_addc_u32 s65, s35, 0
	global_load_lds_dwordx4 v[222:223], off
	s_mov_b32 m0, s37
	v_lshl_add_u64 v[226:227], s[4:5], 0, v[212:213]
	global_load_lds_dwordx4 v210, s[64:65]
	s_mov_b32 m0, s41
	s_nop 0
	global_load_lds_dwordx4 v212, s[64:65]
	v_lshl_add_u64 v[224:225], s[4:5], 0, v[210:211]
	s_mov_b32 m0, s21
	s_nop 0
	global_load_lds_dwordx4 v[224:225], off
	s_mov_b32 m0, s43
	s_nop 0
	global_load_lds_dwordx4 v[226:227], off
	s_cmp_eq_u32 s100, 3
	s_cbranch_scc1 .Lp4vg_w11_a2
	s_cmp_eq_u32 s100, 2
	s_cbranch_scc1 .Lp4vg_wk2_a2
	s_waitcnt vmcnt(8)
	s_branch .Lp4vg_wd_a2

.Lp4vg_wd_a2:
	s_waitcnt lgkmcnt(0)
	s_barrier
	s_setprio 1
	s_waitcnt lgkmcnt(0)
	v_mfma_f32_16x16x32_bf16 v[74:77], v[158:161], v[174:177], v[74:77]
	v_mfma_f32_16x16x32_bf16 v[70:73], v[166:169], v[174:177], v[70:73]
	v_mfma_f32_16x16x32_bf16 v[62:65], v[158:161], v[182:185], v[62:65]
	v_mfma_f32_16x16x32_bf16 v[58:61], v[166:169], v[182:185], v[58:61]
	v_mfma_f32_16x16x32_bf16 v[46:49], v[158:161], v[190:193], v[46:49]
	v_mfma_f32_16x16x32_bf16 v[42:45], v[166:169], v[190:193], v[42:45]
	v_mfma_f32_16x16x32_bf16 v[30:33], v[158:161], v[198:201], v[30:33]
	v_mfma_f32_16x16x32_bf16 v[26:29], v[166:169], v[198:201], v[26:29]
	v_mfma_f32_16x16x32_bf16 v[74:77], v[162:165], v[178:181], v[74:77]
	v_mfma_f32_16x16x32_bf16 v[70:73], v[170:173], v[178:181], v[70:73]
	v_mfma_f32_16x16x32_bf16 v[62:65], v[162:165], v[186:189], v[62:65]
	v_mfma_f32_16x16x32_bf16 v[58:61], v[170:173], v[186:189], v[58:61]
	v_mfma_f32_16x16x32_bf16 v[46:49], v[162:165], v[194:197], v[46:49]
	v_mfma_f32_16x16x32_bf16 v[42:45], v[170:173], v[194:197], v[42:45]
	v_mfma_f32_16x16x32_bf16 v[30:33], v[162:165], v[202:205], v[30:33]
	v_mfma_f32_16x16x32_bf16 v[26:29], v[170:173], v[202:205], v[26:29]
	s_setprio 0
	s_setprio 1
	v_mfma_f32_16x16x32_bf16 v[66:69], v[142:145], v[174:177], v[66:69]
	v_mfma_f32_16x16x32_bf16 v[54:57], v[150:153], v[174:177], v[54:57]
	v_mfma_f32_16x16x32_bf16 v[50:53], v[142:145], v[182:185], v[50:53]
	v_mfma_f32_16x16x32_bf16 v[38:41], v[150:153], v[182:185], v[38:41]
	v_mfma_f32_16x16x32_bf16 v[34:37], v[142:145], v[190:193], v[34:37]
	v_mfma_f32_16x16x32_bf16 v[22:25], v[150:153], v[190:193], v[22:25]
	v_mfma_f32_16x16x32_bf16 v[18:21], v[142:145], v[198:201], v[18:21]
	v_mfma_f32_16x16x32_bf16 v[14:17], v[150:153], v[198:201], v[14:17]
	v_mfma_f32_16x16x32_bf16 v[66:69], v[146:149], v[178:181], v[66:69]
	v_mfma_f32_16x16x32_bf16 v[54:57], v[154:157], v[178:181], v[54:57]
	v_mfma_f32_16x16x32_bf16 v[50:53], v[146:149], v[186:189], v[50:53]
	v_mfma_f32_16x16x32_bf16 v[38:41], v[154:157], v[186:189], v[38:41]
	v_mfma_f32_16x16x32_bf16 v[34:37], v[146:149], v[194:197], v[34:37]
	v_mfma_f32_16x16x32_bf16 v[22:25], v[154:157], v[194:197], v[22:25]
	v_mfma_f32_16x16x32_bf16 v[18:21], v[146:149], v[202:205], v[18:21]
	v_mfma_f32_16x16x32_bf16 v[14:17], v[154:157], v[202:205], v[14:17]
	s_setprio 0
	s_barrier
	v_add_u32_e32 v2, 0x18000, v1
	ds_read_b128 v[158:161], v2
	ds_read_b128 v[162:165], v2 offset:1024
	ds_read_b128 v[166:169], v2 offset:2048
	ds_read_b128 v[170:173], v2 offset:3072
	v_add_u32_e32 v2, 0x1c000, v1
	ds_read_b128 v[142:145], v2
	ds_read_b128 v[146:149], v2 offset:1024
	ds_read_b128 v[150:153], v2 offset:2048
	ds_read_b128 v[154:157], v2 offset:3072
	s_add_u32 s4, s4, 0x80000
	s_addc_u32 s5, s5, 0
	s_mov_b32 m0, s44
	ds_read_b128 v[198:201], v230 offset:32768
	ds_read_b128 v[202:205], v230 offset:33792
	ds_read_b128 v[190:193], v230 offset:34816
	ds_read_b128 v[194:197], v230 offset:35840
	ds_read_b128 v[182:185], v230 offset:36864
	ds_read_b128 v[186:189], v230 offset:37888
	ds_read_b128 v[174:177], v230 offset:38912
	ds_read_b128 v[178:181], v230 offset:39936
	global_load_lds_dwordx4 v210, s[4:5]
	v_lshl_add_u64 v[232:233], s[4:5], 0, v[212:213]
	s_mov_b32 m0, s46
	s_nop 0
	global_load_lds_dwordx4 v[232:233], off
	s_cmp_eq_u32 s100, 3
	s_cbranch_scc1 .Lp4vg_w11_b1
	s_cmp_eq_u32 s100, 2
	s_cbranch_scc1 .Lp4vg_wk2_b1
	s_waitcnt vmcnt(8)
	s_branch .Lp4vg_wd_b1

.LBB0_782:
	ds_read_b64_tr_b16 v[26:27], v228 offset:0
	ds_read_b64_tr_b16 v[28:29], v228 offset:1024
	ds_read_b64_tr_b16 v[30:31], v228 offset:8192
	ds_read_b64_tr_b16 v[32:33], v228 offset:9216
	ds_read_b64_tr_b16 v[18:19], v232 offset:0
	ds_read_b64_tr_b16 v[20:21], v232 offset:1024
	ds_read_b64_tr_b16 v[22:23], v232 offset:8192
	ds_read_b64_tr_b16 v[24:25], v232 offset:9216
	ds_read_b64_tr_b16 v[10:11], v229 offset:0
	ds_read_b64_tr_b16 v[12:13], v229 offset:1024
	ds_read_b64_tr_b16 v[14:15], v229 offset:8192
	ds_read_b64_tr_b16 v[16:17], v229 offset:9216
	ds_read_b64_tr_b16 v[2:3], v233 offset:0
	ds_read_b64_tr_b16 v[4:5], v233 offset:1024
	ds_read_b64_tr_b16 v[6:7], v233 offset:8192
	ds_read_b64_tr_b16 v[8:9], v233 offset:9216
	s_add_i32 m0, s15, 0xc000
	s_nop 0
	ds_read_b128 v[58:61], v236
	ds_read_b128 v[62:65], v236 offset:1024
	ds_read_b128 v[50:53], v236 offset:2048
	ds_read_b128 v[54:57], v236 offset:3072
	ds_read_b128 v[42:45], v236 offset:4096
	ds_read_b128 v[46:49], v236 offset:5120
	ds_read_b128 v[34:37], v236 offset:6144
	ds_read_b128 v[38:41], v236 offset:7168
	global_load_lds_dwordx4 v220, s[42:43]
	s_add_i32 m0, s15, 0xe000
	s_nop 0
	global_load_lds_dwordx4 v222, s[42:43]
	s_cmp_eq_u32 s100, 3
	s_cbranch_scc1 .Lp7vg_w11_a1
	s_cmp_eq_u32 s100, 2
	s_cbranch_scc1 .Lp7vg_wk2_a1
	s_waitcnt vmcnt(8)
	s_branch .Lp7vg_wd_a1

.Lp7vg_mmjoin_a:
	s_barrier
	s_add_u32 s2, s44, 0x1000
	s_addc_u32 s3, s45, 0
	s_mov_b32 m0, s19
	s_nop 0
	global_load_lds_dwordx4 v214, s[44:45]
	s_mov_b32 m0, s33
	s_nop 0
	global_load_lds_dwordx4 v218, s[44:45]
	s_mov_b32 m0, s37
	v_lshl_add_u64 v[224:225], s[4:5], 0, v[216:217]
	global_load_lds_dwordx4 v214, s[2:3]
	s_mov_b32 m0, s39
	v_cndmask_b32_e64 v66, 0, 1, s[40:41]
	global_load_lds_dwordx4 v218, s[2:3]
	s_andn2_b64 vcc, exec, s[40:41]
	s_cbranch_vccnz .Lhalfskip_p7a
	ds_read_b128 v[58:61], v236 offset:16384
	ds_read_b128 v[62:65], v236 offset:17408
	ds_read_b128 v[50:53], v236 offset:18432
	ds_read_b128 v[54:57], v236 offset:19456
	ds_read_b128 v[42:45], v236 offset:20480
	ds_read_b128 v[46:49], v236 offset:21504
	ds_read_b128 v[34:37], v236 offset:22528
	ds_read_b128 v[38:41], v236 offset:23552

.LBB0_790:
	s_barrier
	ds_read_b64_tr_b16 v[26:27], v230 offset:0
	ds_read_b64_tr_b16 v[28:29], v230 offset:1024
	ds_read_b64_tr_b16 v[30:31], v230 offset:8192
	ds_read_b64_tr_b16 v[32:33], v230 offset:9216
	ds_read_b64_tr_b16 v[18:19], v234 offset:0
	ds_read_b64_tr_b16 v[20:21], v234 offset:1024
	ds_read_b64_tr_b16 v[22:23], v234 offset:8192
	ds_read_b64_tr_b16 v[24:25], v234 offset:9216
	ds_read_b64_tr_b16 v[10:11], v231 offset:0
	ds_read_b64_tr_b16 v[12:13], v231 offset:1024
	ds_read_b64_tr_b16 v[14:15], v231 offset:8192
	ds_read_b64_tr_b16 v[16:17], v231 offset:9216
	ds_read_b64_tr_b16 v[2:3], v235 offset:0
	ds_read_b64_tr_b16 v[4:5], v235 offset:1024
	ds_read_b64_tr_b16 v[6:7], v235 offset:8192
	ds_read_b64_tr_b16 v[8:9], v235 offset:9216
	s_add_u32 s4, s4, 0x40000
	s_addc_u32 s5, s5, 0
	s_mov_b32 m0, s50
	s_nop 0
	ds_read_b128 v[58:61], v236 offset:32768
	ds_read_b128 v[62:65], v236 offset:33792
	ds_read_b128 v[50:53], v236 offset:34816
	ds_read_b128 v[54:57], v236 offset:35840
	ds_read_b128 v[42:45], v236 offset:36864
	ds_read_b128 v[46:49], v236 offset:37888
	ds_read_b128 v[34:37], v236 offset:38912
	ds_read_b128 v[38:41], v236 offset:39936
	global_load_lds_dwordx4 v212, s[4:5]
	s_mov_b32 m0, s51
	s_nop 0
	global_load_lds_dwordx4 v216, s[4:5]
	s_cmp_eq_u32 s100, 3
	s_cbranch_scc1 .Lp7vg_w11_b1
	s_cmp_eq_u32 s100, 2
	s_cbranch_scc1 .Lp7vg_wk2_b1
	s_waitcnt vmcnt(8)
	s_branch .Lp7vg_wd_b1

.Lp7vg_mmjoin_b:
	s_barrier
	s_add_i32 m0, s15, 0x18000
	s_nop 0
	global_load_lds_dwordx4 v214, s[46:47]
	s_add_i32 m0, s15, 0x1a000
	s_nop 0
	global_load_lds_dwordx4 v218, s[46:47]
	s_add_u32 s44, s44, 0x85000
	s_addc_u32 s45, s45, 0
	s_add_i32 m0, s15, 0x1c000
	v_lshl_add_u64 v[68:69], v[68:69], 0, s[10:11]
	global_load_lds_dwordx4 v214, s[44:45]
	s_add_i32 m0, s15, 0x1e000
	s_nop 0
	global_load_lds_dwordx4 v218, s[44:45]
	s_and_b64 vcc, exec, s[2:3]
	s_cbranch_vccnz .Lhalfskip_p7b
	ds_read_b128 v[58:61], v236 offset:49152
	ds_read_b128 v[62:65], v236 offset:50176
	ds_read_b128 v[50:53], v236 offset:51200
	ds_read_b128 v[54:57], v236 offset:52224
	ds_read_b128 v[42:45], v236 offset:53248
	ds_read_b128 v[46:49], v236 offset:54272
	ds_read_b128 v[34:37], v236 offset:55296
	ds_read_b128 v[38:41], v236 offset:56320

.LBB0_901:
	ds_read_b64_tr_b16 v[26:27], v207 offset:0
	ds_read_b64_tr_b16 v[28:29], v207 offset:1024
	ds_read_b64_tr_b16 v[30:31], v207 offset:8192
	ds_read_b64_tr_b16 v[32:33], v207 offset:9216
	ds_read_b64_tr_b16 v[18:19], v217 offset:0
	ds_read_b64_tr_b16 v[20:21], v217 offset:1024
	ds_read_b64_tr_b16 v[22:23], v217 offset:8192
	ds_read_b64_tr_b16 v[24:25], v217 offset:9216
	ds_read_b64_tr_b16 v[10:11], v214 offset:0
	ds_read_b64_tr_b16 v[12:13], v214 offset:1024
	ds_read_b64_tr_b16 v[14:15], v214 offset:8192
	ds_read_b64_tr_b16 v[16:17], v214 offset:9216
	ds_read_b64_tr_b16 v[2:3], v218 offset:0
	ds_read_b64_tr_b16 v[4:5], v218 offset:1024
	ds_read_b64_tr_b16 v[6:7], v218 offset:8192
	ds_read_b64_tr_b16 v[8:9], v218 offset:9216
	s_add_u32 s2, s50, 0xfffc0080
	s_addc_u32 s3, s51, -1
	s_cmp_eq_u32 s72, 12
	s_cselect_b32 s55, s29, s3
	s_cselect_b32 s54, s31, s2
	s_cselect_b32 s53, s35, s71
	s_cselect_b32 s52, s43, s70
	ds_read_b128 v[34:37], v223
	ds_read_b128 v[38:41], v223 offset:1024
	ds_read_b128 v[42:45], v223 offset:2048
	ds_read_b128 v[46:49], v223 offset:3072
	ds_read_b128 v[50:53], v223 offset:4096
	ds_read_b128 v[54:57], v223 offset:5120
	ds_read_b128 v[58:61], v223 offset:6144
	ds_read_b128 v[62:65], v223 offset:7168
	s_waitcnt vmcnt(6)
	s_waitcnt lgkmcnt(0)
	s_barrier
	s_setprio 1
	s_waitcnt lgkmcnt(0)
	v_mfma_scale_f32_16x16x128_f8f6f4 v[194:197], v[26:33], v[34:41], v[194:197], v1, v1 op_sel_hi:[0,0,0]
	v_mfma_scale_f32_16x16x128_f8f6f4 v[190:193], v[18:25], v[34:41], v[190:193], v1, v1 op_sel_hi:[0,0,0]
	v_mfma_scale_f32_16x16x128_f8f6f4 v[186:189], v[26:33], v[42:49], v[186:189], v1, v1 op_sel_hi:[0,0,0]
	v_mfma_scale_f32_16x16x128_f8f6f4 v[182:185], v[18:25], v[42:49], v[182:185], v1, v1 op_sel_hi:[0,0,0]
	s_add_i32 m0, s17, 0xc000
	s_nop 0
	global_load_lds_dwordx4 v208, s[50:51]
	v_mfma_scale_f32_16x16x128_f8f6f4 v[162:165], v[26:33], v[50:57], v[162:165], v1, v1 op_sel_hi:[0,0,0]
	v_mfma_scale_f32_16x16x128_f8f6f4 v[158:161], v[18:25], v[50:57], v[158:161], v1, v1 op_sel_hi:[0,0,0]
	v_mfma_scale_f32_16x16x128_f8f6f4 v[146:149], v[26:33], v[58:65], v[146:149], v1, v1 op_sel_hi:[0,0,0]
	v_mfma_scale_f32_16x16x128_f8f6f4 v[142:145], v[18:25], v[58:65], v[142:145], v1, v1 op_sel_hi:[0,0,0]
	s_setprio 0
	s_setprio 1
	v_mfma_scale_f32_16x16x128_f8f6f4 v[178:181], v[10:17], v[34:41], v[178:181], v1, v1 op_sel_hi:[0,0,0]
	v_mfma_scale_f32_16x16x128_f8f6f4 v[174:177], v[2:9], v[34:41], v[174:177], v1, v1 op_sel_hi:[0,0,0]
	s_add_i32 m0, s17, 0xe000
	s_nop 0
	global_load_lds_dwordx4 v210, s[50:51]
	v_mfma_scale_f32_16x16x128_f8f6f4 v[170:173], v[10:17], v[42:49], v[170:173], v1, v1 op_sel_hi:[0,0,0]
	v_mfma_scale_f32_16x16x128_f8f6f4 v[166:169], v[2:9], v[42:49], v[166:169], v1, v1 op_sel_hi:[0,0,0]
	v_mfma_scale_f32_16x16x128_f8f6f4 v[154:157], v[10:17], v[50:57], v[154:157], v1, v1 op_sel_hi:[0,0,0]
	v_mfma_scale_f32_16x16x128_f8f6f4 v[150:153], v[2:9], v[50:57], v[150:153], v1, v1 op_sel_hi:[0,0,0]
	v_mfma_scale_f32_16x16x128_f8f6f4 v[138:141], v[10:17], v[58:65], v[138:141], v1, v1 op_sel_hi:[0,0,0]
	v_mfma_scale_f32_16x16x128_f8f6f4 v[134:137], v[2:9], v[58:65], v[134:137], v1, v1 op_sel_hi:[0,0,0]
	s_setprio 0
	s_barrier
	s_mov_b32 m0, s19
	v_lshl_add_u64 v[68:69], s[52:53], 0, v[200:201]
	global_load_lds_dwordx4 v[68:69], off
	v_lshl_add_u64 v[212:213], s[52:53], 0, v[204:205]
	s_mov_b32 m0, s33
	v_lshl_add_u64 v[68:69], v[68:69], 0, s[4:5]
	global_load_lds_dwordx4 v[212:213], off
	s_mov_b32 m0, s45
	s_nop 0
	global_load_lds_dwordx4 v[68:69], off
	v_lshl_add_u64 v[68:69], v[212:213], 0, s[4:5]
	s_mov_b32 m0, s47
	v_lshl_add_u64 v[212:213], s[54:55], 0, v[202:203]
	global_load_lds_dwordx4 v[68:69], off
	s_andn2_b64 vcc, exec, s[48:49]
	s_cbranch_vccnz .Lhalfskip_p8a
	ds_read_b128 v[58:61], v223 offset:16384
	ds_read_b128 v[62:65], v223 offset:17408
	ds_read_b128 v[50:53], v223 offset:18432
	ds_read_b128 v[54:57], v223 offset:19456
	ds_read_b128 v[42:45], v223 offset:20480
	ds_read_b128 v[46:49], v223 offset:21504
	ds_read_b128 v[34:37], v223 offset:22528
	ds_read_b128 v[38:41], v223 offset:23552

.LBB0_903:
	s_add_u32 s56, s52, 0x40000
	s_addc_u32 s57, s53, 0
	s_barrier
	ds_read_b64_tr_b16 v[26:27], v215 offset:0
	ds_read_b64_tr_b16 v[28:29], v215 offset:1024
	ds_read_b64_tr_b16 v[30:31], v215 offset:8192
	ds_read_b64_tr_b16 v[32:33], v215 offset:9216
	ds_read_b64_tr_b16 v[18:19], v219 offset:0
	ds_read_b64_tr_b16 v[20:21], v219 offset:1024
	ds_read_b64_tr_b16 v[22:23], v219 offset:8192
	ds_read_b64_tr_b16 v[24:25], v219 offset:9216
	ds_read_b64_tr_b16 v[10:11], v216 offset:0
	ds_read_b64_tr_b16 v[12:13], v216 offset:1024
	ds_read_b64_tr_b16 v[14:15], v216 offset:8192
	ds_read_b64_tr_b16 v[16:17], v216 offset:9216
	ds_read_b64_tr_b16 v[2:3], v220 offset:0
	ds_read_b64_tr_b16 v[4:5], v220 offset:1024
	ds_read_b64_tr_b16 v[6:7], v220 offset:8192
	ds_read_b64_tr_b16 v[8:9], v220 offset:9216
	s_add_u32 s54, s54, 0x40000
	s_addc_u32 s55, s55, 0
	ds_read_b128 v[34:37], v223 offset:32768
	ds_read_b128 v[38:41], v223 offset:33792
	ds_read_b128 v[42:45], v223 offset:34816
	ds_read_b128 v[46:49], v223 offset:35840
	ds_read_b128 v[50:53], v223 offset:36864
	ds_read_b128 v[54:57], v223 offset:37888
	ds_read_b128 v[58:61], v223 offset:38912
	ds_read_b128 v[62:65], v223 offset:39936
	s_waitcnt vmcnt(6)
	s_waitcnt lgkmcnt(0)
	s_barrier
	s_setprio 1
	s_waitcnt lgkmcnt(0)
	v_mfma_scale_f32_16x16x128_f8f6f4 v[194:197], v[26:33], v[34:41], v[194:197], v1, v1 op_sel_hi:[0,0,0]
	v_mfma_scale_f32_16x16x128_f8f6f4 v[190:193], v[18:25], v[34:41], v[190:193], v1, v1 op_sel_hi:[0,0,0]
	v_mfma_scale_f32_16x16x128_f8f6f4 v[186:189], v[26:33], v[42:49], v[186:189], v1, v1 op_sel_hi:[0,0,0]
	v_mfma_scale_f32_16x16x128_f8f6f4 v[182:185], v[18:25], v[42:49], v[182:185], v1, v1 op_sel_hi:[0,0,0]
	s_mov_b32 m0, s59
	s_nop 0
	global_load_lds_dwordx4 v198, s[54:55]
	v_mfma_scale_f32_16x16x128_f8f6f4 v[162:165], v[26:33], v[50:57], v[162:165], v1, v1 op_sel_hi:[0,0,0]
	v_mfma_scale_f32_16x16x128_f8f6f4 v[158:161], v[18:25], v[50:57], v[158:161], v1, v1 op_sel_hi:[0,0,0]
	v_mfma_scale_f32_16x16x128_f8f6f4 v[146:149], v[26:33], v[58:65], v[146:149], v1, v1 op_sel_hi:[0,0,0]
	v_mfma_scale_f32_16x16x128_f8f6f4 v[142:145], v[18:25], v[58:65], v[142:145], v1, v1 op_sel_hi:[0,0,0]
	s_setprio 0
	s_setprio 1
	v_mfma_scale_f32_16x16x128_f8f6f4 v[178:181], v[10:17], v[34:41], v[178:181], v1, v1 op_sel_hi:[0,0,0]
	v_mfma_scale_f32_16x16x128_f8f6f4 v[174:177], v[2:9], v[34:41], v[174:177], v1, v1 op_sel_hi:[0,0,0]
	s_mov_b32 m0, s60
	s_nop 0
	global_load_lds_dwordx4 v202, s[54:55]
	v_mfma_scale_f32_16x16x128_f8f6f4 v[170:173], v[10:17], v[42:49], v[170:173], v1, v1 op_sel_hi:[0,0,0]
	v_mfma_scale_f32_16x16x128_f8f6f4 v[166:169], v[2:9], v[42:49], v[166:169], v1, v1 op_sel_hi:[0,0,0]
	v_mfma_scale_f32_16x16x128_f8f6f4 v[154:157], v[10:17], v[50:57], v[154:157], v1, v1 op_sel_hi:[0,0,0]
	v_mfma_scale_f32_16x16x128_f8f6f4 v[150:153], v[2:9], v[50:57], v[150:153], v1, v1 op_sel_hi:[0,0,0]
	v_mfma_scale_f32_16x16x128_f8f6f4 v[138:141], v[10:17], v[58:65], v[138:141], v1, v1 op_sel_hi:[0,0,0]
	v_mfma_scale_f32_16x16x128_f8f6f4 v[134:137], v[2:9], v[58:65], v[134:137], v1, v1 op_sel_hi:[0,0,0]
	s_setprio 0
	s_barrier
	s_add_i32 m0, s17, 0x18000
	s_nop 0
	global_load_lds_dwordx4 v200, s[56:57]
	s_add_i32 m0, s17, 0x1a000
	s_nop 0
	global_load_lds_dwordx4 v204, s[56:57]
	s_add_u32 s52, s52, 0x40100
	s_addc_u32 s53, s53, 0
	s_add_i32 m0, s17, 0x1c000
	v_lshl_add_u64 v[68:69], v[68:69], 0, s[12:13]
	global_load_lds_dwordx4 v200, s[52:53]
	s_add_i32 m0, s17, 0x1e000
	s_nop 0
	global_load_lds_dwordx4 v204, s[52:53]
	s_and_b64 vcc, exec, s[2:3]
	s_cbranch_vccnz .Lhalfskip_p8b
	ds_read_b128 v[58:61], v223 offset:49152
	ds_read_b128 v[62:65], v223 offset:50176
	ds_read_b128 v[50:53], v223 offset:51200
	ds_read_b128 v[54:57], v223 offset:52224
	ds_read_b128 v[42:45], v223 offset:53248
	ds_read_b128 v[46:49], v223 offset:54272
	ds_read_b128 v[34:37], v223 offset:55296
	ds_read_b128 v[38:41], v223 offset:56320
